# baseline (speedup 1.0000x reference)
.LBB1_3:
	ds_read_b128 v[128:131], v126 offset:49152
	ds_read_b128 v[132:135], v126 offset:50176
	ds_read_b128 v[136:139], v126 offset:51200
	ds_read_b128 v[140:143], v126 offset:52224
	s_add_u32 s30, s16, s0
	s_addc_u32 s31, s17, s1
	ds_read_b128 v[144:147], v110
	ds_read_b128 v[148:151], v110 offset:1024
	ds_read_b128 v[152:155], v109
	ds_read_b128 v[156:159], v109 offset:1024
	ds_read_b128 v[160:163], v108
	ds_read_b128 v[164:167], v108 offset:1024
	s_mov_b32 s34, s60
	s_add_u32 s52, s30, s18
	s_addc_u32 s53, s31, s19
	s_mov_b32 m0, s34
	s_nop 0
	global_load_lds_dwordx4 v100, s[52:53]
	s_mov_b32 s34, s61
	s_add_u32 s52, s30, s18
	s_addc_u32 s53, s31, s19
	s_mov_b32 m0, s34
	s_nop 0
	global_load_lds_dwordx4 v101, s[52:53]
	s_waitcnt lgkmcnt(6)
	s_barrier
	s_waitcnt lgkmcnt(0)
	s_setprio 0
	s_waitcnt lgkmcnt(0)
	v_mfma_f32_16x16x32_f16 v[94:97], v[144:147], v[128:131], v[94:97]
	v_mfma_f32_16x16x32_f16 v[90:93], v[144:147], v[136:139], v[90:93]
	v_mfma_f32_16x16x32_f16 v[86:89], v[152:155], v[128:131], v[86:89]
	v_mfma_f32_16x16x32_f16 v[82:85], v[152:155], v[136:139], v[82:85]
	v_mfma_f32_16x16x32_f16 v[78:81], v[160:163], v[128:131], v[78:81]
	v_mfma_f32_16x16x32_f16 v[74:77], v[160:163], v[136:139], v[74:77]
	v_mfma_f32_16x16x32_f16 v[94:97], v[148:151], v[132:135], v[94:97]
	v_mfma_f32_16x16x32_f16 v[90:93], v[148:151], v[140:143], v[90:93]
	v_mfma_f32_16x16x32_f16 v[86:89], v[156:159], v[132:135], v[86:89]
	v_mfma_f32_16x16x32_f16 v[82:85], v[156:159], v[140:143], v[82:85]
	v_mfma_f32_16x16x32_f16 v[78:81], v[164:167], v[132:135], v[78:81]
	v_mfma_f32_16x16x32_f16 v[74:77], v[164:167], v[140:143], v[74:77]
	s_setprio 1
	s_barrier
	s_add_u32 s34, s2, s0
	s_addc_u32 s35, s3, s1
	ds_read_b128 v[168:171], v122
	ds_read_b128 v[172:175], v122 offset:1024
	ds_read_b128 v[176:179], v122 offset:2048
	ds_read_b128 v[180:183], v122 offset:3072
	s_mov_b32 s42, s62
	s_add_u32 s54, s34, s20
	s_addc_u32 s55, s35, s21
	s_mov_b32 m0, s42
	s_nop 0
	global_load_lds_dwordx4 v100, s[54:55]
	s_mov_b32 s42, s63
	s_add_u32 s54, s34, s20
	s_addc_u32 s55, s35, s21
	s_mov_b32 m0, s42
	s_nop 0
	global_load_lds_dwordx4 v103, s[54:55]
	s_barrier
	s_waitcnt lgkmcnt(0)
	s_setprio 0
	s_waitcnt lgkmcnt(0)
	v_mfma_f32_16x16x32_f16 v[70:73], v[144:147], v[168:171], v[70:73]
	v_mfma_f32_16x16x32_f16 v[66:69], v[144:147], v[176:179], v[66:69]
	v_mfma_f32_16x16x32_f16 v[62:65], v[152:155], v[168:171], v[62:65]
	v_mfma_f32_16x16x32_f16 v[50:53], v[152:155], v[176:179], v[50:53]
	v_mfma_f32_16x16x32_f16 v[46:49], v[160:163], v[168:171], v[46:49]
	v_mfma_f32_16x16x32_f16 v[42:45], v[160:163], v[176:179], v[42:45]
	v_mfma_f32_16x16x32_f16 v[70:73], v[148:151], v[172:175], v[70:73]
	v_mfma_f32_16x16x32_f16 v[66:69], v[148:151], v[180:183], v[66:69]
	v_mfma_f32_16x16x32_f16 v[62:65], v[156:159], v[172:175], v[62:65]
	v_mfma_f32_16x16x32_f16 v[50:53], v[156:159], v[180:183], v[50:53]
	v_mfma_f32_16x16x32_f16 v[46:49], v[164:167], v[172:175], v[46:49]
	v_mfma_f32_16x16x32_f16 v[42:45], v[164:167], v[180:183], v[42:45]
	s_setprio 1
	s_barrier
	ds_read_b128 v[144:147], v110 offset:12288
	ds_read_b128 v[148:151], v110 offset:13312
	ds_read_b128 v[152:155], v109 offset:12288
	ds_read_b128 v[156:159], v109 offset:13312
	ds_read_b128 v[160:163], v108 offset:12288
	ds_read_b128 v[164:167], v108 offset:13312
	s_mov_b32 s42, s64
	s_add_u32 s54, s30, s20
	s_addc_u32 s55, s31, s21
	s_mov_b32 m0, s42
	s_nop 0
	global_load_lds_dwordx4 v100, s[54:55]
	s_mov_b32 s42, s65
	s_add_u32 s54, s30, s20
	s_addc_u32 s55, s31, s21
	s_mov_b32 m0, s42
	s_nop 0
	global_load_lds_dwordx4 v101, s[54:55]
	s_barrier
	s_waitcnt lgkmcnt(0)
	s_setprio 0
	s_waitcnt lgkmcnt(0)
	v_mfma_f32_16x16x32_f16 v[38:41], v[144:147], v[128:131], v[38:41]
	v_mfma_f32_16x16x32_f16 v[34:37], v[144:147], v[136:139], v[34:37]
	v_mfma_f32_16x16x32_f16 v[30:33], v[152:155], v[128:131], v[30:33]
	v_mfma_f32_16x16x32_f16 v[26:29], v[152:155], v[136:139], v[26:29]
	v_mfma_f32_16x16x32_f16 v[22:25], v[160:163], v[128:131], v[22:25]
	v_mfma_f32_16x16x32_f16 v[18:21], v[160:163], v[136:139], v[18:21]
	v_mfma_f32_16x16x32_f16 v[38:41], v[148:151], v[132:135], v[38:41]
	v_mfma_f32_16x16x32_f16 v[34:37], v[148:151], v[140:143], v[34:37]
	v_mfma_f32_16x16x32_f16 v[30:33], v[156:159], v[132:135], v[30:33]
	v_mfma_f32_16x16x32_f16 v[26:29], v[156:159], v[140:143], v[26:29]
	v_mfma_f32_16x16x32_f16 v[22:25], v[164:167], v[132:135], v[22:25]
	v_mfma_f32_16x16x32_f16 v[18:21], v[164:167], v[140:143], v[18:21]
	s_setprio 1
	s_barrier
	s_mov_b32 s42, s66
	s_add_u32 s56, s34, s22
	s_addc_u32 s57, s35, s23
	s_mov_b32 m0, s42
	s_nop 0
	global_load_lds_dwordx4 v100, s[56:57]
	s_mov_b32 s42, s67
	s_add_u32 s56, s34, s22
	s_addc_u32 s57, s35, s23
	s_mov_b32 m0, s42
	s_nop 0
	global_load_lds_dwordx4 v103, s[56:57]
	s_waitcnt vmcnt(6)
	s_barrier
	s_setprio 0
	v_mfma_f32_16x16x32_f16 v[14:17], v[144:147], v[168:171], v[14:17]
	v_mfma_f32_16x16x32_f16 v[10:13], v[144:147], v[176:179], v[10:13]
	v_mfma_f32_16x16x32_f16 v[6:9], v[152:155], v[168:171], v[6:9]
	v_mfma_f32_16x16x32_f16 v[2:5], v[152:155], v[176:179], v[2:5]
	v_mfma_f32_16x16x32_f16 v[54:57], v[160:163], v[168:171], v[54:57]
	v_mfma_f32_16x16x32_f16 v[58:61], v[160:163], v[176:179], v[58:61]
	v_mfma_f32_16x16x32_f16 v[14:17], v[148:151], v[172:175], v[14:17]
	v_mfma_f32_16x16x32_f16 v[10:13], v[148:151], v[180:183], v[10:13]
	v_mfma_f32_16x16x32_f16 v[6:9], v[156:159], v[172:175], v[6:9]
	v_mfma_f32_16x16x32_f16 v[2:5], v[156:159], v[180:183], v[2:5]
	v_mfma_f32_16x16x32_f16 v[54:57], v[164:167], v[172:175], v[54:57]
	v_mfma_f32_16x16x32_f16 v[58:61], v[164:167], v[180:183], v[58:61]
	s_setprio 1
	s_barrier
	ds_read_b128 v[128:131], v117
	ds_read_b128 v[132:135], v117 offset:1024
	ds_read_b128 v[136:139], v117 offset:2048
	ds_read_b128 v[140:143], v117 offset:3072
	ds_read_b128 v[144:147], v110 offset:24576
	ds_read_b128 v[148:151], v110 offset:25600
	ds_read_b128 v[152:155], v109 offset:24576
	ds_read_b128 v[156:159], v109 offset:25600
	ds_read_b128 v[160:163], v108 offset:24576
	ds_read_b128 v[164:167], v108 offset:25600
	s_mov_b32 s42, s68
	s_add_u32 s52, s30, s24
	s_addc_u32 s53, s31, s25
	s_mov_b32 m0, s42
	s_nop 0
	global_load_lds_dwordx4 v100, s[52:53]
	s_mov_b32 s42, s69
	s_add_u32 s52, s30, s24
	s_addc_u32 s53, s31, s25
	s_mov_b32 m0, s42
	s_nop 0
	global_load_lds_dwordx4 v101, s[52:53]
	s_waitcnt lgkmcnt(6)
	s_barrier
	s_waitcnt lgkmcnt(0)
	s_setprio 0
	s_waitcnt lgkmcnt(0)
	v_mfma_f32_16x16x32_f16 v[94:97], v[144:147], v[128:131], v[94:97]
	v_mfma_f32_16x16x32_f16 v[90:93], v[144:147], v[136:139], v[90:93]
	v_mfma_f32_16x16x32_f16 v[86:89], v[152:155], v[128:131], v[86:89]
	v_mfma_f32_16x16x32_f16 v[82:85], v[152:155], v[136:139], v[82:85]
	v_mfma_f32_16x16x32_f16 v[78:81], v[160:163], v[128:131], v[78:81]
	v_mfma_f32_16x16x32_f16 v[74:77], v[160:163], v[136:139], v[74:77]
	v_mfma_f32_16x16x32_f16 v[94:97], v[148:151], v[132:135], v[94:97]
	v_mfma_f32_16x16x32_f16 v[90:93], v[148:151], v[140:143], v[90:93]
	v_mfma_f32_16x16x32_f16 v[86:89], v[156:159], v[132:135], v[86:89]
	v_mfma_f32_16x16x32_f16 v[82:85], v[156:159], v[140:143], v[82:85]
	v_mfma_f32_16x16x32_f16 v[78:81], v[164:167], v[132:135], v[78:81]
	v_mfma_f32_16x16x32_f16 v[74:77], v[164:167], v[140:143], v[74:77]
	s_setprio 1
	s_barrier
	ds_read_b128 v[168:171], v114
	ds_read_b128 v[172:175], v114 offset:1024
	ds_read_b128 v[176:179], v114 offset:2048
	ds_read_b128 v[180:183], v114 offset:3072
	s_mov_b32 s42, s70
	s_add_u32 s54, s34, s26
	s_addc_u32 s55, s35, s27
	s_mov_b32 m0, s42
	s_nop 0
	global_load_lds_dwordx4 v100, s[54:55]
	s_mov_b32 s42, s71
	s_add_u32 s54, s34, s26
	s_addc_u32 s55, s35, s27
	s_mov_b32 m0, s42
	s_nop 0
	global_load_lds_dwordx4 v103, s[54:55]
	s_barrier
	s_waitcnt lgkmcnt(0)
	s_setprio 0
	s_waitcnt lgkmcnt(0)
	v_mfma_f32_16x16x32_f16 v[70:73], v[144:147], v[168:171], v[70:73]
	v_mfma_f32_16x16x32_f16 v[66:69], v[144:147], v[176:179], v[66:69]
	v_mfma_f32_16x16x32_f16 v[62:65], v[152:155], v[168:171], v[62:65]
	v_mfma_f32_16x16x32_f16 v[50:53], v[152:155], v[176:179], v[50:53]
	v_mfma_f32_16x16x32_f16 v[46:49], v[160:163], v[168:171], v[46:49]
	v_mfma_f32_16x16x32_f16 v[42:45], v[160:163], v[176:179], v[42:45]
	v_mfma_f32_16x16x32_f16 v[70:73], v[148:151], v[172:175], v[70:73]
	v_mfma_f32_16x16x32_f16 v[66:69], v[148:151], v[180:183], v[66:69]
	v_mfma_f32_16x16x32_f16 v[62:65], v[156:159], v[172:175], v[62:65]
	v_mfma_f32_16x16x32_f16 v[50:53], v[156:159], v[180:183], v[50:53]
	v_mfma_f32_16x16x32_f16 v[46:49], v[164:167], v[172:175], v[46:49]
	v_mfma_f32_16x16x32_f16 v[42:45], v[164:167], v[180:183], v[42:45]
	s_setprio 1
	s_barrier
	ds_read_b128 v[144:147], v110 offset:36864
	ds_read_b128 v[148:151], v110 offset:37888
	ds_read_b128 v[152:155], v109 offset:36864
	ds_read_b128 v[156:159], v109 offset:37888
	ds_read_b128 v[160:163], v108 offset:36864
	ds_read_b128 v[164:167], v108 offset:37888
	s_mov_b32 s42, s72
	s_add_u32 s54, s30, s26
	s_addc_u32 s55, s31, s27
	s_mov_b32 m0, s42
	s_nop 0
	global_load_lds_dwordx4 v100, s[54:55]
	s_nop 0
	s_add_u32 s54, s30, s26
	s_addc_u32 s55, s31, s27
	s_mov_b32 s30, s73
	s_mov_b32 m0, s30
	s_nop 0
	global_load_lds_dwordx4 v101, s[54:55]
	s_barrier
	s_waitcnt lgkmcnt(0)
	s_setprio 0
	s_waitcnt lgkmcnt(0)
	v_mfma_f32_16x16x32_f16 v[38:41], v[144:147], v[128:131], v[38:41]
	v_mfma_f32_16x16x32_f16 v[34:37], v[144:147], v[136:139], v[34:37]
	v_mfma_f32_16x16x32_f16 v[30:33], v[152:155], v[128:131], v[30:33]
	v_mfma_f32_16x16x32_f16 v[26:29], v[152:155], v[136:139], v[26:29]
	v_mfma_f32_16x16x32_f16 v[22:25], v[160:163], v[128:131], v[22:25]
	v_mfma_f32_16x16x32_f16 v[18:21], v[160:163], v[136:139], v[18:21]
	v_mfma_f32_16x16x32_f16 v[38:41], v[148:151], v[132:135], v[38:41]
	v_mfma_f32_16x16x32_f16 v[34:37], v[148:151], v[140:143], v[34:37]
	v_mfma_f32_16x16x32_f16 v[30:33], v[156:159], v[132:135], v[30:33]
	v_mfma_f32_16x16x32_f16 v[26:29], v[156:159], v[140:143], v[26:29]
	v_mfma_f32_16x16x32_f16 v[22:25], v[164:167], v[132:135], v[22:25]
	v_mfma_f32_16x16x32_f16 v[18:21], v[164:167], v[140:143], v[18:21]
	s_setprio 1
	s_barrier
	s_mov_b32 s30, s74
	s_add_u32 s56, s34, s28
	s_addc_u32 s57, s35, s29
	s_mov_b32 m0, s30
	s_nop 0
	global_load_lds_dwordx4 v100, s[56:57]
	s_mov_b32 s30, s75
	s_add_u32 s56, s34, s28
	s_addc_u32 s57, s35, s29
	s_mov_b32 m0, s30
	s_nop 0
	global_load_lds_dwordx4 v103, s[56:57]
	s_waitcnt vmcnt(6)
	s_barrier
	s_setprio 0
	v_mfma_f32_16x16x32_f16 v[14:17], v[144:147], v[168:171], v[14:17]
	v_mfma_f32_16x16x32_f16 v[10:13], v[144:147], v[176:179], v[10:13]
	v_mfma_f32_16x16x32_f16 v[6:9], v[152:155], v[168:171], v[6:9]
	v_mfma_f32_16x16x32_f16 v[2:5], v[152:155], v[176:179], v[2:5]
	v_mfma_f32_16x16x32_f16 v[54:57], v[160:163], v[168:171], v[54:57]
	v_mfma_f32_16x16x32_f16 v[58:61], v[160:163], v[176:179], v[58:61]
	v_mfma_f32_16x16x32_f16 v[14:17], v[148:151], v[172:175], v[14:17]
	v_mfma_f32_16x16x32_f16 v[10:13], v[148:151], v[180:183], v[10:13]
	v_mfma_f32_16x16x32_f16 v[6:9], v[156:159], v[172:175], v[6:9]
	v_mfma_f32_16x16x32_f16 v[2:5], v[156:159], v[180:183], v[2:5]
	v_mfma_f32_16x16x32_f16 v[54:57], v[164:167], v[172:175], v[54:57]
	v_mfma_f32_16x16x32_f16 v[58:61], v[164:167], v[180:183], v[58:61]
	s_setprio 1
	s_add_i32 s41, s41, 2
	s_add_u32 s0, s0, 0x100
	s_addc_u32 s1, s1, 0
	s_cmp_lt_u32 s41, 12
	s_barrier
	s_cbranch_scc1 .LBB1_3
	v_add_u32_e32 v98, 0x9000, v1
	s_add_u32 s0, s16, 0x30780
	v_readfirstlane_b32 s2, v98
	s_addc_u32 s1, s17, 0
	s_mov_b32 m0, s2
	v_readfirstlane_b32 s2, v125
	ds_read_b128 v[118:121], v126 offset:49152
	ds_read_b128 v[128:131], v126 offset:50176
	ds_read_b128 v[132:135], v126 offset:51200
	ds_read_b128 v[136:139], v126 offset:52224
	ds_read_b128 v[140:143], v110
	ds_read_b128 v[144:147], v110 offset:1024
	ds_read_b128 v[148:151], v109
	ds_read_b128 v[152:155], v109 offset:1024
	ds_read_b128 v[156:159], v108
	ds_read_b128 v[160:163], v108 offset:1024
	s_nop 0
	global_load_lds_dwordx4 v100, s[0:1]
	s_mov_b32 m0, s2
	s_nop 0
	global_load_lds_dwordx4 v101, s[0:1]
	s_barrier
	s_waitcnt lgkmcnt(0)
	s_setprio 0
	s_waitcnt lgkmcnt(0)
	v_mfma_f32_16x16x32_f16 v[90:93], v[140:143], v[132:135], v[90:93]
	v_mfma_f32_16x16x32_f16 v[86:89], v[148:151], v[118:121], v[86:89]
	v_mfma_f32_16x16x32_f16 v[82:85], v[148:151], v[132:135], v[82:85]
	v_mfma_f32_16x16x32_f16 v[94:97], v[140:143], v[118:121], v[94:97]
	v_mfma_f32_16x16x32_f16 v[90:93], v[144:147], v[136:139], v[90:93]
	v_mfma_f32_16x16x32_f16 v[86:89], v[152:155], v[128:131], v[86:89]
	v_mfma_f32_16x16x32_f16 v[82:85], v[152:155], v[136:139], v[82:85]
	v_mfma_f32_16x16x32_f16 v[78:81], v[156:159], v[118:121], v[78:81]
	v_mfma_f32_16x16x32_f16 v[74:77], v[156:159], v[132:135], v[74:77]
	v_mfma_f32_16x16x32_f16 v[94:97], v[144:147], v[128:131], v[94:97]
	v_mfma_f32_16x16x32_f16 v[124:127], v[160:163], v[128:131], v[78:81]
	v_mfma_f32_16x16x32_f16 v[164:167], v[160:163], v[136:139], v[74:77]
	s_setprio 1
	s_barrier
	s_nop 2
	ds_read_b128 v[74:77], v122
	ds_read_b128 v[78:81], v122 offset:1024
	ds_read_b128 v[98:101], v122 offset:2048
	ds_read_b128 v[168:171], v122 offset:3072
	s_barrier
	s_waitcnt lgkmcnt(0)
	s_setprio 0
	s_waitcnt lgkmcnt(0)
	v_mfma_f32_16x16x32_f16 v[70:73], v[140:143], v[74:77], v[70:73]
	v_mfma_f32_16x16x32_f16 v[66:69], v[140:143], v[98:101], v[66:69]
	v_mfma_f32_16x16x32_f16 v[50:53], v[148:151], v[98:101], v[50:53]
	v_mfma_f32_16x16x32_f16 v[46:49], v[156:159], v[74:77], v[46:49]
	v_mfma_f32_16x16x32_f16 v[42:45], v[156:159], v[98:101], v[42:45]
	v_mfma_f32_16x16x32_f16 v[70:73], v[144:147], v[78:81], v[70:73]
	v_mfma_f32_16x16x32_f16 v[66:69], v[144:147], v[168:171], v[66:69]
	v_mfma_f32_16x16x32_f16 v[62:65], v[148:151], v[74:77], v[62:65]
	v_mfma_f32_16x16x32_f16 v[50:53], v[152:155], v[168:171], v[50:53]
	v_mfma_f32_16x16x32_f16 v[46:49], v[160:163], v[78:81], v[46:49]
	v_mfma_f32_16x16x32_f16 v[42:45], v[160:163], v[168:171], v[42:45]
	v_mfma_f32_16x16x32_f16 v[140:143], v[152:155], v[78:81], v[62:65]
	s_setprio 1
	s_barrier
	s_nop 1
	ds_read_b128 v[62:65], v110 offset:12288
	ds_read_b128 v[144:147], v110 offset:13312
	ds_read_b128 v[148:151], v109 offset:12288
	ds_read_b128 v[152:155], v109 offset:13312
	ds_read_b128 v[156:159], v108 offset:12288
	ds_read_b128 v[160:163], v108 offset:13312
	s_waitcnt vmcnt(4)
	s_barrier
	s_waitcnt lgkmcnt(0)
	s_setprio 0
	s_waitcnt lgkmcnt(0)
	v_mfma_f32_16x16x32_f16 v[38:41], v[62:65], v[118:121], v[38:41]
	v_mfma_f32_16x16x32_f16 v[34:37], v[62:65], v[132:135], v[34:37]
	v_mfma_f32_16x16x32_f16 v[30:33], v[148:151], v[118:121], v[30:33]
	v_mfma_f32_16x16x32_f16 v[26:29], v[148:151], v[132:135], v[26:29]
	v_mfma_f32_16x16x32_f16 v[22:25], v[156:159], v[118:121], v[22:25]
	v_mfma_f32_16x16x32_f16 v[18:21], v[156:159], v[132:135], v[18:21]
	v_mfma_f32_16x16x32_f16 v[38:41], v[144:147], v[128:131], v[38:41]
	v_mfma_f32_16x16x32_f16 v[34:37], v[144:147], v[136:139], v[34:37]
	v_mfma_f32_16x16x32_f16 v[30:33], v[152:155], v[128:131], v[30:33]
	v_mfma_f32_16x16x32_f16 v[26:29], v[152:155], v[136:139], v[26:29]
	v_mfma_f32_16x16x32_f16 v[22:25], v[160:163], v[128:131], v[22:25]
	v_mfma_f32_16x16x32_f16 v[18:21], v[160:163], v[136:139], v[18:21]
	s_setprio 1
	s_setprio 0
	v_mfma_f32_16x16x32_f16 v[10:13], v[62:65], v[98:101], v[10:13]
	v_mfma_f32_16x16x32_f16 v[128:131], v[144:147], v[168:171], v[10:13]
	v_mfma_f32_16x16x32_f16 v[6:9], v[148:151], v[74:77], v[6:9]
	v_mfma_f32_16x16x32_f16 v[2:5], v[148:151], v[98:101], v[2:5]
	v_mfma_f32_16x16x32_f16 v[10:13], v[156:159], v[74:77], v[54:57]
	v_mfma_f32_16x16x32_f16 v[14:17], v[62:65], v[74:77], v[14:17]
	v_mfma_f32_16x16x32_f16 v[6:9], v[152:155], v[78:81], v[6:9]
	v_mfma_f32_16x16x32_f16 v[2:5], v[152:155], v[168:171], v[2:5]
	v_mfma_f32_16x16x32_f16 v[132:135], v[160:163], v[78:81], v[10:13]
	v_mfma_f32_16x16x32_f16 v[10:13], v[156:159], v[98:101], v[58:61]
	v_mfma_f32_16x16x32_f16 v[118:121], v[144:147], v[78:81], v[14:17]
	v_mfma_f32_16x16x32_f16 v[136:139], v[160:163], v[168:171], v[10:13]
	s_setprio 1
	s_barrier
	s_nop 3
	ds_read_b128 v[10:13], v117
	ds_read_b128 v[14:17], v117 offset:1024
	ds_read_b128 v[144:147], v117 offset:2048
	ds_read_b128 v[148:151], v117 offset:3072
	ds_read_b128 v[54:57], v110 offset:24576
	ds_read_b128 v[152:155], v110 offset:25600
	ds_read_b128 v[156:159], v109 offset:24576
	ds_read_b128 v[160:163], v109 offset:25600
	ds_read_b128 v[168:171], v108 offset:24576
	ds_read_b128 v[172:175], v108 offset:25600
	s_waitcnt vmcnt(2)
	s_barrier
	s_waitcnt lgkmcnt(0)
	s_setprio 0
	s_waitcnt lgkmcnt(0)
	v_mfma_f32_16x16x32_f16 v[58:61], v[54:57], v[10:13], v[94:97]
	v_mfma_f32_16x16x32_f16 v[98:101], v[152:155], v[14:17], v[58:61]
	v_mfma_f32_16x16x32_f16 v[58:61], v[54:57], v[144:147], v[90:93]
	v_mfma_f32_16x16x32_f16 v[90:93], v[152:155], v[148:151], v[58:61]
	v_mfma_f32_16x16x32_f16 v[58:61], v[156:159], v[10:13], v[86:89]
	v_mfma_f32_16x16x32_f16 v[78:81], v[160:163], v[14:17], v[58:61]
	v_mfma_f32_16x16x32_f16 v[58:61], v[156:159], v[144:147], v[82:85]
	v_mfma_f32_16x16x32_f16 v[74:77], v[160:163], v[148:151], v[58:61]
	v_mfma_f32_16x16x32_f16 v[58:61], v[168:171], v[10:13], v[124:127]
	v_mfma_f32_16x16x32_f16 v[62:65], v[172:175], v[14:17], v[58:61]
	v_mfma_f32_16x16x32_f16 v[58:61], v[168:171], v[144:147], v[164:167]
	v_mfma_f32_16x16x32_f16 v[58:61], v[172:175], v[148:151], v[58:61]
	s_setprio 1
	s_barrier
	ds_read_b128 v[94:97], v114
	ds_read_b128 v[122:125], v114 offset:1024
	ds_read_b128 v[164:167], v114 offset:2048
	ds_read_b128 v[112:115], v114 offset:3072
	s_waitcnt vmcnt(0)
	s_barrier
	s_waitcnt lgkmcnt(0)
	s_setprio 0
	s_waitcnt lgkmcnt(0)
	v_mfma_f32_16x16x32_f16 v[70:73], v[54:57], v[94:97], v[70:73]
	v_mfma_f32_16x16x32_f16 v[54:57], v[54:57], v[164:167], v[66:69]
	v_mfma_f32_16x16x32_f16 v[82:85], v[152:155], v[112:115], v[54:57]
	v_mfma_f32_16x16x32_f16 v[54:57], v[156:159], v[94:97], v[140:143]
	v_mfma_f32_16x16x32_f16 v[50:53], v[156:159], v[164:167], v[50:53]
	v_mfma_f32_16x16x32_f16 v[46:49], v[168:171], v[94:97], v[46:49]
	v_mfma_f32_16x16x32_f16 v[42:45], v[168:171], v[164:167], v[42:45]
	v_mfma_f32_16x16x32_f16 v[86:89], v[152:155], v[122:125], v[70:73]
	v_mfma_f32_16x16x32_f16 v[70:73], v[160:163], v[122:125], v[54:57]
	v_mfma_f32_16x16x32_f16 v[66:69], v[160:163], v[112:115], v[50:53]
	v_mfma_f32_16x16x32_f16 v[54:57], v[172:175], v[122:125], v[46:49]
	v_mfma_f32_16x16x32_f16 v[50:53], v[172:175], v[112:115], v[42:45]
	s_setprio 1
	s_barrier
	ds_read_b128 v[140:143], v110 offset:36864
	ds_read_b128 v[152:155], v110 offset:37888
	ds_read_b128 v[156:159], v109 offset:36864
	ds_read_b128 v[160:163], v109 offset:37888
	ds_read_b128 v[168:171], v108 offset:36864
	ds_read_b128 v[106:109], v108 offset:37888
	s_barrier
	s_waitcnt lgkmcnt(0)
	s_setprio 0
	s_waitcnt lgkmcnt(0)
	v_mfma_f32_16x16x32_f16 v[38:41], v[140:143], v[10:13], v[38:41]
	v_mfma_f32_16x16x32_f16 v[30:33], v[156:159], v[10:13], v[30:33]
	v_mfma_f32_16x16x32_f16 v[10:13], v[168:171], v[10:13], v[22:25]
	v_mfma_f32_16x16x32_f16 v[46:49], v[152:155], v[14:17], v[38:41]
	v_mfma_f32_16x16x32_f16 v[34:37], v[140:143], v[144:147], v[34:37]
	v_mfma_f32_16x16x32_f16 v[30:33], v[160:163], v[14:17], v[30:33]
	v_mfma_f32_16x16x32_f16 v[26:29], v[156:159], v[144:147], v[26:29]
	v_mfma_f32_16x16x32_f16 v[14:17], v[106:109], v[14:17], v[10:13]
	v_mfma_f32_16x16x32_f16 v[10:13], v[168:171], v[144:147], v[18:21]
	v_mfma_f32_16x16x32_f16 v[42:45], v[152:155], v[148:151], v[34:37]
	v_mfma_f32_16x16x32_f16 v[26:29], v[160:163], v[148:151], v[26:29]
	v_mfma_f32_16x16x32_f16 v[10:13], v[106:109], v[148:151], v[10:13]
	s_setprio 1
	s_setprio 0
	v_mfma_f32_16x16x32_f16 v[18:21], v[140:143], v[94:97], v[118:121]
	v_mfma_f32_16x16x32_f16 v[38:41], v[152:155], v[122:125], v[18:21]
	v_mfma_f32_16x16x32_f16 v[18:21], v[140:143], v[164:167], v[128:131]
	v_mfma_f32_16x16x32_f16 v[2:5], v[156:159], v[164:167], v[2:5]
	v_mfma_f32_16x16x32_f16 v[34:37], v[152:155], v[112:115], v[18:21]
	v_mfma_f32_16x16x32_f16 v[6:9], v[156:159], v[94:97], v[6:9]
	v_mfma_f32_16x16x32_f16 v[18:21], v[160:163], v[112:115], v[2:5]
	v_mfma_f32_16x16x32_f16 v[2:5], v[168:171], v[94:97], v[132:135]
	v_mfma_f32_16x16x32_f16 v[22:25], v[160:163], v[122:125], v[6:9]
	v_mfma_f32_16x16x32_f16 v[6:9], v[106:109], v[122:125], v[2:5]
	v_mfma_f32_16x16x32_f16 v[2:5], v[168:171], v[164:167], v[136:139]
	v_mfma_f32_16x16x32_f16 v[2:5], v[106:109], v[112:115], v[2:5]
	s_setprio 1
	s_andn2_b64 vcc, exec, vcc
	s_barrier
	s_cbranch_vccnz .LBB1_6
	s_barrier
